# K-fragment prefetch depth in MoBA QK, tail share retune, no sleep in barrier spin
# baseline (speedup 1.0000x reference)
.LBB0_116:
	v_mov_b32_e32 v2, v0
	s_mov_b32 s0, s35
	s_mov_b32 s8, s45
	v_readfirstlane_b32 s6, v2
	s_ashr_i32 s7, s6, 6
	s_add_i32 s9, s8, 0xffffff80
	s_add_i32 s10, s0, 0xffffff80
	s_cmpk_gt_i32 s8, 0x7f
	s_cselect_b64 s[4:5], -1, 0
	s_and_b64 s[0:1], s[4:5], exec
	s_cselect_b32 s8, s9, s8
	s_movk_i32 s1, 0x1600
	s_cselect_b32 s12, s10, 0x80
	s_cselect_b32 s0, 0, 0xe14
	s_cselect_b32 s1, 0xe14, s1
	s_lshl_b32 s9, s8, 3
	v_readlane_b32 s10, v248, 17
	s_cmp_eq_u32 s10, 2
	s_movk_i32 s10, 0x6e00
	s_cselect_b32 s10, s10, 0x5800
	s_add_i32 s11, s7, s10
	v_and_b32_e32 v37, 63, v2
	s_add_i32 s0, s11, s0
	s_add_i32 s0, s0, s9
	s_add_i32 s1, s1, s10
	v_lshlrev_b32_e32 v38, 2, v37
	s_cmp_ge_i32 s0, s1
	v_and_b32_e32 v112, 28, v38
	s_mov_b32 s46, 0xf800000
	s_cbranch_scc1 .LBB0_121
	v_readlane_b32 s10, v248, 13
	s_lshl_b32 s9, s12, 3
	s_lshl_b32 s10, s10, 1
	v_readlane_b32 s14, v248, 15
	v_readlane_b32 s15, v248, 16
	s_add_u32 s11, s14, 0x5800000
	s_addc_u32 s13, s15, 0
	v_and_b32_e32 v36, 56, v2
	s_branch .LBB0_119

.LBB0_121:
	v_readlane_b32 s0, v248, 11
	s_cmp_lt_u32 s0, 9
	v_readlane_b32 s0, v248, 17
	s_cselect_b32 s9, 0x108, 0
	s_cmp_lg_u32 s0, 0
	s_cselect_b64 s[0:1], -1, 0
	s_and_b64 s[10:11], s[0:1], exec
	s_cselect_b32 s9, s9, 0x100
	s_mul_i32 s10, s9, 0x100
	s_lshr_b32 s10, s10, 8
	s_and_b64 s[4:5], s[4:5], exec
	s_cselect_b32 s4, 0, s10
	s_cselect_b32 s13, s10, s9
	s_add_i32 s14, s4, s8
	s_cmp_ge_i32 s14, s13
	s_cbranch_scc1 .LBB0_153
	s_lshl_b32 s4, s7, 14
	v_readlane_b32 s27, v248, 13
	s_add_i32 s15, s4, 0
	s_add_i32 s4, s27, 1
	s_mul_i32 s5, s4, 0xa400000
	v_readlane_b32 s8, v250, 34
	v_readlane_b32 s64, v250, 4
	s_add_u32 s8, s8, s5
	v_readlane_b32 s5, v250, 35
	v_readlane_b32 s65, v250, 5
	v_readlane_b32 s66, v250, 6
	v_readlane_b32 s67, v250, 7
	v_readlane_b32 s68, v250, 8
	v_readlane_b32 s69, v250, 9
	v_readlane_b32 s70, v250, 10
	v_readlane_b32 s71, v250, 11
	v_readlane_b32 s72, v250, 12
	v_readlane_b32 s73, v250, 13
	v_readlane_b32 s74, v250, 14
	v_readlane_b32 s75, v250, 15
	s_addc_u32 s9, s5, 0
	s_mul_i32 s4, s4, 0x2c00000
	s_mov_b32 s5, s60
	v_readlane_b32 s76, v250, 16
	v_readlane_b32 s77, v250, 17
	v_readlane_b32 s78, v250, 18
	v_readlane_b32 s79, v250, 19
	s_mov_b64 s[64:65], s[68:69]
	s_lshl_b64 s[4:5], s[4:5], 2
	s_mov_b64 s[66:67], s[70:71]
	s_mov_b64 s[68:69], s[72:73]
	s_mov_b64 s[70:71], s[74:75]
	s_add_u32 s4, s70, s4
	s_mul_i32 s26, s27, 0x6000
	s_addc_u32 s5, s71, s5
	s_add_i32 s10, s26, 0x6000
	s_add_u32 s24, s64, s10
	s_addc_u32 s25, s65, 0
	s_lshl_b32 s10, s7, 8
	s_ashr_i32 s11, s10, 31
	v_and_b32_e32 v4, 0xe0, v38
	s_lshl_b64 s[22:23], s[10:11], 2
	v_or_b32_e32 v6, s10, v4
	v_mov_b64_e32 v[8:9], s[4:5]
	s_mov_b32 s4, 0xb000
	s_add_u32 s24, s24, s22
	v_mad_i64_i32 v[8:9], s[4:5], v6, s4, v[8:9]
	s_addc_u32 s25, s25, s23
	s_lshl_b32 s4, s7, 7
	v_readlane_b32 s5, v249, 50
	s_add_i32 s4, s5, s4
	v_lshlrev_b32_e32 v2, 4, v37
	v_lshlrev_b32_e32 v10, 2, v112
	s_cmp_lt_u32 s6, 64
	v_mov_b32_e32 v11, v3
	v_cmp_gt_u32_e64 s[36:37], 8, v37
	v_add_u32_e32 v191, s4, v2
	v_add_u32_e32 v192, s5, v10
	s_cselect_b64 s[4:5], -1, 0
	v_lshl_add_u64 v[124:125], v[8:9], 0, v[10:11]
	s_and_b64 s[4:5], s[36:37], s[4:5]
	v_lshl_add_u64 v[8:9], s[8:9], 0, v[10:11]
	s_mov_b64 s[6:7], 0x2000000
	v_lshl_add_u64 v[126:127], v[8:9], 0, s[6:7]
	s_add_u32 s6, s8, s10
	s_mov_b64 s[72:73], s[76:77]
	s_mov_b64 s[74:75], s[78:79]
	v_readlane_b32 s76, v249, 55
	s_addc_u32 s7, s9, s11
	v_mov_b32_e32 v5, v3
	v_readlane_b32 s78, v249, 57
	v_lshl_add_u64 v[128:129], s[6:7], 0, v[4:5]
	s_lshl_b32 s6, s27, 24
	v_readlane_b32 s79, v249, 58
	v_ashrrev_i32_e32 v7, 31, v6
	s_add_u32 s6, s78, s6
	s_addc_u32 s7, s79, 0
	v_lshlrev_b64 v[8:9], 13, v[6:7]
	v_readlane_b32 s8, v248, 15
	v_lshl_add_u64 v[8:9], s[6:7], 0, v[8:9]
	v_readlane_b32 s9, v248, 16
	v_lshl_add_u64 v[130:131], v[8:9], 0, v[10:11]
	s_mov_b64 s[6:7], 0xa200000
	v_lshl_add_u64 v[8:9], s[8:9], 0, v[10:11]
	v_lshl_add_u64 v[132:133], v[8:9], 0, s[6:7]
	s_add_u32 s6, s8, s10
	s_addc_u32 s7, s9, s11
	v_lshl_add_u32 v190, v4, 2, s15
	v_lshl_add_u64 v[4:5], s[6:7], 0, v[4:5]
	s_mov_b64 s[6:7], 0x9c00000
	v_lshl_add_u64 v[134:135], v[4:5], 0, s[6:7]
	s_lshl_b32 s6, s27, 23
	v_readlane_b32 s77, v249, 56
	s_add_u32 s6, s76, s6
	s_addc_u32 s7, s77, 0
	s_lshl_b32 s8, s27, 13
	s_add_u32 s8, s68, s8
	s_addc_u32 s9, s69, 0
	s_add_u32 s8, s8, s22
	s_addc_u32 s9, s9, s23
	v_lshl_add_u64 v[136:137], s[8:9], 0, v[2:3]
	s_mul_i32 s8, s27, 0x2800000
	s_mul_hi_u32 s9, s27, 0x2800000
	s_add_u32 s8, s74, s8
	s_addc_u32 s9, s75, s9
	s_add_u32 s10, s64, s26
	s_addc_u32 s11, s65, 0
	s_add_u32 s10, s10, s22
	s_addc_u32 s11, s11, s23
	v_lshl_add_u64 v[12:13], s[10:11], 0, v[2:3]
	s_mov_b64 s[10:11], 0x2000
	v_lshl_add_u64 v[138:139], v[12:13], 0, s[10:11]
	v_mov_b64_e32 v[12:13], s[8:9]
	s_movk_i32 s8, 0x5000
	v_mad_i64_i32 v[12:13], s[8:9], v6, s8, v[12:13]
	s_mov_b64 s[8:9], 0x9400000
	v_readlane_b32 s80, v249, 59
	v_readlane_b32 s81, v249, 60
	v_lshl_add_u64 v[142:143], v[8:9], 0, s[8:9]
	s_mov_b64 s[8:9], 0x8400000
	v_readlane_b32 s72, v248, 9
	v_readlane_b32 s80, v248, 1
	v_readlane_b32 s78, v249, 63
	v_readlane_b32 s76, v250, 22
	v_readlane_b32 s26, v248, 5
	v_lshl_add_u64 v[144:145], v[4:5], 0, s[8:9]
	v_lshlrev_b64 v[4:5], 12, v[6:7]
	v_readlane_b32 s73, v248, 10
	v_readlane_b32 s82, v249, 61
	v_readlane_b32 s83, v249, 62
	v_readlane_b32 s81, v248, 2
	v_lshl_add_u64 v[122:123], s[24:25], 0, v[2:3]
	v_add_u32_e32 v113, s15, v2
	v_readlane_b32 s79, v248, 0
	v_readlane_b32 s77, v250, 23
	v_readlane_b32 s27, v248, 6
	v_lshl_add_u64 v[140:141], v[12:13], 0, v[10:11]
	v_lshl_add_u64 v[146:147], s[6:7], 0, v[4:5]
	s_lshl_b32 s6, s14, 5
	s_lshl_b32 s15, s12, 5
	s_branch .LBB0_125

.LBB0_157:
	v_readlane_b32 s4, v250, 40
	v_readlane_b32 s5, v250, 41
	global_load_dword v4, v3, s[84:85] sc1
	global_load_dword v2, v3, s[26:27] sc1
	s_mov_b64 s[6:7], -1
	s_waitcnt vmcnt(0)
	v_add_u32_e32 v19, v2, v4
	global_load_dword v5, v3, s[4:5] sc1
	v_readlane_b32 s4, v250, 42
	v_readlane_b32 s5, v250, 43
	s_waitcnt vmcnt(0)
	v_add_u32_e32 v19, v19, v5
	s_nop 2
	global_load_dword v6, v3, s[4:5] sc1
	v_readlane_b32 s4, v250, 44
	v_readlane_b32 s5, v250, 45
	s_waitcnt vmcnt(0)
	v_add_u32_e32 v19, v19, v6
	s_nop 2
	global_load_dword v7, v3, s[4:5] sc1
	v_readlane_b32 s4, v250, 46
	v_readlane_b32 s5, v250, 47
	s_waitcnt vmcnt(0)
	v_add_u32_e32 v19, v19, v7
	s_nop 2
	global_load_dword v8, v3, s[4:5] sc1
	v_readlane_b32 s4, v250, 48
	v_readlane_b32 s5, v250, 49
	s_waitcnt vmcnt(0)
	v_add_u32_e32 v19, v19, v8
	s_nop 2
	global_load_dword v9, v3, s[4:5] sc1
	v_readlane_b32 s4, v250, 50
	v_readlane_b32 s5, v250, 51
	s_waitcnt vmcnt(0)
	v_add_u32_e32 v19, v19, v9
	s_nop 2
	global_load_dword v10, v3, s[4:5] sc1
	v_readlane_b32 s4, v250, 52
	v_readlane_b32 s5, v250, 53
	s_waitcnt vmcnt(0)
	v_add_u32_e32 v19, v19, v10
	s_nop 2
	global_load_dword v11, v3, s[4:5] sc1
	v_readlane_b32 s4, v250, 54
	v_readlane_b32 s5, v250, 55
	s_waitcnt vmcnt(0)
	v_add_u32_e32 v19, v19, v11
	s_nop 2
	global_load_dword v12, v3, s[4:5] sc1
	v_readlane_b32 s4, v250, 56
	v_readlane_b32 s5, v250, 57
	s_waitcnt vmcnt(0)
	v_add_u32_e32 v19, v19, v12
	s_nop 2
	global_load_dword v13, v3, s[4:5] sc1
	v_readlane_b32 s4, v250, 58
	v_readlane_b32 s5, v250, 59
	s_waitcnt vmcnt(0)
	v_add_u32_e32 v19, v19, v13
	s_nop 2
	global_load_dword v14, v3, s[4:5] sc1
	v_readlane_b32 s4, v250, 60
	v_readlane_b32 s5, v250, 61
	s_waitcnt vmcnt(0)
	v_add_u32_e32 v19, v19, v14
	s_nop 2
	global_load_dword v15, v3, s[4:5] sc1
	v_readlane_b32 s4, v250, 62
	v_readlane_b32 s5, v250, 63
	s_waitcnt vmcnt(0)
	v_add_u32_e32 v19, v19, v15
	s_nop 2
	global_load_dword v16, v3, s[4:5] sc1
	v_readlane_b32 s4, v249, 0
	v_readlane_b32 s5, v249, 1
	s_waitcnt vmcnt(0)
	v_add_u32_e32 v19, v19, v16
	s_nop 2
	global_load_dword v17, v3, s[4:5] sc1
	v_readlane_b32 s4, v249, 2
	v_readlane_b32 s5, v249, 3
	s_waitcnt vmcnt(0)
	v_add_u32_e32 v19, v19, v17
	s_nop 2
	global_load_dword v18, v3, s[4:5] sc1
	s_mov_b64 s[4:5], -1
	s_waitcnt vmcnt(0)
	v_add_u32_e32 v19, v19, v18
	v_cmp_eq_u32_e32 vcc, s10, v19
	s_cbranch_vccnz .LBB0_156
	s_and_b32 s4, s11, 0xff
	s_cmp_eq_u32 s4, 0
	s_mov_b64 s[4:5], -1
	s_mov_b64 s[8:9], -1
	s_nop 0
	s_cbranch_scc0 .LBB0_161
	v_readlane_b32 s4, v250, 38
	v_readlane_b32 s5, v250, 39
	s_nop 4
	global_load_dword v19, v3, s[4:5] sc1
	s_waitcnt vmcnt(0)
	v_cmp_eq_u32_e32 vcc, 0, v19
	s_cbranch_vccnz .LBB0_163
	s_mov_b64 s[8:9], 0
	s_mov_b64 s[4:5], -1

.LBB0_173:
	s_and_b32 s14, s22, 0xff
	s_mov_b64 s[12:13], -1
	s_cmp_lg_u32 s14, 0
	s_mov_b64 s[36:37], -1
	s_nop 0
	s_cbranch_scc1 .LBB0_176
	v_readlane_b32 s14, v250, 38
	v_readlane_b32 s15, v250, 39
	s_nop 4
	global_load_dword v4, v3, s[14:15] sc1
	s_waitcnt vmcnt(0)
	v_cmp_eq_u32_e32 vcc, 0, v4
	s_cbranch_vccnz .LBB0_178
	s_mov_b64 s[36:37], 0
	s_mov_b64 s[14:15], -1

.LBB0_579:
	v_readlane_b32 s6, v250, 40
	v_readlane_b32 s7, v250, 41
	global_load_dword v4, v3, s[84:85] sc1
	global_load_dword v2, v3, s[26:27] sc1
	s_mov_b64 s[8:9], -1
	s_waitcnt vmcnt(0)
	v_add_u32_e32 v19, v2, v4
	global_load_dword v5, v3, s[6:7] sc1
	v_readlane_b32 s6, v250, 42
	v_readlane_b32 s7, v250, 43
	s_waitcnt vmcnt(0)
	v_add_u32_e32 v19, v19, v5
	s_nop 2
	global_load_dword v6, v3, s[6:7] sc1
	v_readlane_b32 s6, v250, 44
	v_readlane_b32 s7, v250, 45
	s_waitcnt vmcnt(0)
	v_add_u32_e32 v19, v19, v6
	s_nop 2
	global_load_dword v7, v3, s[6:7] sc1
	v_readlane_b32 s6, v250, 46
	v_readlane_b32 s7, v250, 47
	s_waitcnt vmcnt(0)
	v_add_u32_e32 v19, v19, v7
	s_nop 2
	global_load_dword v8, v3, s[6:7] sc1
	v_readlane_b32 s6, v250, 48
	v_readlane_b32 s7, v250, 49
	s_waitcnt vmcnt(0)
	v_add_u32_e32 v19, v19, v8
	s_nop 2
	global_load_dword v9, v3, s[6:7] sc1
	v_readlane_b32 s6, v250, 50
	v_readlane_b32 s7, v250, 51
	s_waitcnt vmcnt(0)
	v_add_u32_e32 v19, v19, v9
	s_nop 2
	global_load_dword v10, v3, s[6:7] sc1
	v_readlane_b32 s6, v250, 52
	v_readlane_b32 s7, v250, 53
	s_waitcnt vmcnt(0)
	v_add_u32_e32 v19, v19, v10
	s_nop 2
	global_load_dword v11, v3, s[6:7] sc1
	v_readlane_b32 s6, v250, 54
	v_readlane_b32 s7, v250, 55
	s_waitcnt vmcnt(0)
	v_add_u32_e32 v19, v19, v11
	s_nop 2
	global_load_dword v12, v3, s[6:7] sc1
	v_readlane_b32 s6, v250, 56
	v_readlane_b32 s7, v250, 57
	s_waitcnt vmcnt(0)
	v_add_u32_e32 v19, v19, v12
	s_nop 2
	global_load_dword v13, v3, s[6:7] sc1
	v_readlane_b32 s6, v250, 58
	v_readlane_b32 s7, v250, 59
	s_waitcnt vmcnt(0)
	v_add_u32_e32 v19, v19, v13
	s_nop 2
	global_load_dword v14, v3, s[6:7] sc1
	v_readlane_b32 s6, v250, 60
	v_readlane_b32 s7, v250, 61
	s_waitcnt vmcnt(0)
	v_add_u32_e32 v19, v19, v14
	s_nop 2
	global_load_dword v15, v3, s[6:7] sc1
	v_readlane_b32 s6, v250, 62
	v_readlane_b32 s7, v250, 63
	s_waitcnt vmcnt(0)
	v_add_u32_e32 v19, v19, v15
	s_nop 2
	global_load_dword v16, v3, s[6:7] sc1
	v_readlane_b32 s6, v249, 0
	v_readlane_b32 s7, v249, 1
	s_waitcnt vmcnt(0)
	v_add_u32_e32 v19, v19, v16
	s_nop 2
	global_load_dword v17, v3, s[6:7] sc1
	v_readlane_b32 s6, v249, 2
	v_readlane_b32 s7, v249, 3
	s_waitcnt vmcnt(0)
	v_add_u32_e32 v19, v19, v17
	s_nop 2
	global_load_dword v18, v3, s[6:7] sc1
	s_mov_b64 s[6:7], -1
	s_waitcnt vmcnt(0)
	v_add_u32_e32 v19, v19, v18
	v_cmp_eq_u32_e32 vcc, s12, v19
	s_cbranch_vccnz .LBB0_578
	s_and_b32 s6, s13, 0xff
	s_cmp_eq_u32 s6, 0
	s_mov_b64 s[6:7], -1
	s_mov_b64 s[10:11], -1
	s_nop 0
	s_cbranch_scc0 .LBB0_583
	v_readlane_b32 s6, v250, 38
	v_readlane_b32 s7, v250, 39
	s_nop 4
	global_load_dword v19, v3, s[6:7] sc1
	s_waitcnt vmcnt(0)
	v_cmp_eq_u32_e32 vcc, 0, v19
	s_cbranch_vccnz .LBB0_585
	s_mov_b64 s[10:11], 0
	s_mov_b64 s[6:7], -1

.LBB0_595:
	s_and_b32 s23, s22, 0xff
	s_mov_b64 s[14:15], -1
	s_cmp_lg_u32 s23, 0
	s_mov_b64 s[38:39], -1
	s_nop 0
	s_cbranch_scc1 .LBB0_598
	v_readlane_b32 s24, v250, 38
	v_readlane_b32 s25, v250, 39
	s_nop 4
	global_load_dword v4, v3, s[24:25] sc1
	s_waitcnt vmcnt(0)
	v_cmp_eq_u32_e32 vcc, 0, v4
	s_cbranch_vccnz .LBB0_600
	s_mov_b64 s[38:39], 0
	s_mov_b64 s[36:37], -1
